# static priority: layer-kernel prologue and GEMM/epilogue phases at s_setprio 3, gather loop at 0 (the opposite assignment cost +16 us)
# speedup vs baseline: 1.0025x; 1.0025x over previous
_Z12layer_kernelILb1ELi512ELi64EEvPKDv8_DF16_PKfPS0_PiS6_S6_S2_S4_S5_PfPK15HIP_vector_typeIiLj2EEPKi:
	s_setprio 3
	s_load_dword s3, s[0:1], 0x60
	s_load_dwordx2 s[4:5], s[0:1], 0x58
	s_load_dwordx2 s[44:45], s[0:1], 0x38
	s_load_dwordx2 s[24:25], s[0:1], 0x0
	s_waitcnt lgkmcnt(0)
	s_ashr_i32 s6, s3, 3
	s_and_b32 s7, s3, 7
	s_and_b32 s3, s2, 7
	s_add_i32 s10, s6, 1
	s_cmp_ge_u32 s3, s7
	s_cbranch_scc0 .LBB4_2
	s_mul_i32 s8, s10, s7
	s_sub_i32 s7, s3, s7
	s_mul_i32 s7, s7, s6
	s_add_i32 s11, s8, s7
	s_cbranch_execz .LBB4_3
	s_branch .LBB4_4

.LBB4_45:
	s_setprio 0
	v_or_b32_e32 v17, 1, v31
	v_add_u32_e32 v14, s30, v17
	v_min_i32_e32 v14, 0x1869f, v14
	v_lshl_add_u32 v14, v14, 8, v26
	global_load_dwordx4 v[10:13], v14, s[24:25]
	s_mov_b64 s[28:29], exec
	s_movk_i32 s0, 0x4400
	v_subrev_u32_e32 v1, s20, v32
	v_lshl_add_u32 v1, v1, 2, s0
	v_lshl_add_u32 v16, v32, 8, v26
	v_cmp_lt_i32_e64 s[2:3], v32, v33
	v_add_u32_e32 v14, 1, v32
	v_cmp_lt_i32_e64 s[8:9], v14, v33
	s_mov_b64 exec, s[2:3]
	ds_read_b32 v18, v1
	ds_read_b32 v19, v1 offset:4096
	s_waitcnt lgkmcnt(0)
	v_lshl_add_u32 v18, v18, 9, v26
	v_lshl_add_u32 v19, v19, 8, v26
	global_load_dwordx4 v[34:37], v18, s[4:5] offset:256 nt
	global_load_dwordx4 v[20:23], v18, s[4:5] nt
	global_load_dwordx4 v[38:41], v19, s[24:25]
	ds_read_b32 v18, v1 offset:8
	ds_read_b32 v19, v1 offset:4104
	s_mov_b64 exec, s[8:9]
	ds_read_b32 v24, v1 offset:4
	ds_read_b32 v25, v1 offset:4100
	s_waitcnt lgkmcnt(0)
	v_lshl_add_u32 v24, v24, 9, v26
	v_lshl_add_u32 v25, v25, 8, v26
	global_load_dwordx4 v[50:53], v24, s[4:5] offset:256 nt
	global_load_dwordx4 v[46:49], v24, s[4:5] nt
	global_load_dwordx4 v[54:57], v25, s[24:25]
	ds_read_b32 v24, v1 offset:12
	ds_read_b32 v25, v1 offset:4108
	s_mov_b64 exec, s[28:29]
	s_cmp_eq_u64 s[2:3], 0
	s_cbranch_scc1 .Ll0_p1_empty
	s_waitcnt vmcnt(3)
	s_branch .Ll0_p1_body

.LBB4_70:
	s_setprio 3
	v_lshlrev_b32_e32 v2, 4, v0
	global_load_dwordx4 v[6:9], v2, s[18:19]
	v_mov_b32_e32 v3, 0
	v_lshl_add_u64 v[22:23], s[18:19], 0, v[2:3]
	v_add_co_u32_e32 v2, vcc, 0x2000, v22
	v_cvt_pk_f16_f32 v17, v16, v17
	s_nop 0
	v_addc_co_u32_e32 v3, vcc, 0, v23, vcc
	s_waitcnt lgkmcnt(0)
	global_load_dwordx4 v[18:21], v[2:3], off
	v_add_co_u32_e32 v2, vcc, 0x4000, v22
	v_cvt_pk_f16_f32 v16, v14, v15
	s_nop 0
	v_addc_co_u32_e32 v3, vcc, 0, v23, vcc
	global_load_dwordx4 v[2:5], v[2:3], off
	v_cvt_pk_f16_f32 v14, v10, v11
	s_movk_i32 s2, 0x110
	v_add_co_u32_e32 v10, vcc, 0x6000, v22
	v_cvt_pk_f16_f32 v15, v12, v13
	v_mad_u32_u24 v1, v1, s2, v26
	v_addc_co_u32_e32 v11, vcc, 0, v23, vcc
	ds_write_b128 v1, v[14:17]
	global_load_dwordx4 v[14:17], v[10:11], off
	v_and_b32_e32 v27, 48, v0
	v_mad_u32_u24 v40, v42, s2, v27
	s_waitcnt lgkmcnt(0)
	s_barrier
	ds_read_b128 v[10:13], v40
	ds_read_b128 v[22:25], v40 offset:64
	ds_read_b128 v[28:31], v40 offset:4352
	ds_read_b128 v[32:35], v40 offset:4416
	ds_read_b128 v[36:39], v40 offset:8704
	ds_read_b128 v[44:47], v40 offset:8768
	ds_read_b128 v[48:51], v40 offset:13056
	ds_read_b128 v[52:55], v40 offset:13120
	v_mbcnt_hi_u32_b32 v1, -1, v43
	s_waitcnt vmcnt(3) lgkmcnt(7)
	v_mfma_f32_16x16x32_f16 v[10:13], v[10:13], v[6:9], 0
	s_waitcnt lgkmcnt(5)
	v_mfma_f32_16x16x32_f16 v[28:31], v[28:31], v[6:9], 0
	s_waitcnt lgkmcnt(3)
	v_mfma_f32_16x16x32_f16 v[36:39], v[36:39], v[6:9], 0
	s_waitcnt lgkmcnt(1)
	v_mfma_f32_16x16x32_f16 v[6:9], v[48:51], v[6:9], 0
	s_waitcnt vmcnt(2)
	v_mfma_f32_16x16x32_f16 v[10:13], v[22:25], v[18:21], v[10:13]
	v_mfma_f32_16x16x32_f16 v[22:25], v[32:35], v[18:21], v[28:31]
	v_mfma_f32_16x16x32_f16 v[28:31], v[44:47], v[18:21], v[36:39]
	s_waitcnt lgkmcnt(0)
	v_mfma_f32_16x16x32_f16 v[6:9], v[52:55], v[18:21], v[6:9]
	ds_read_b128 v[18:21], v40 offset:128
	ds_read_b128 v[32:35], v40 offset:192
	s_waitcnt vmcnt(1) lgkmcnt(1)
	v_mfma_f32_16x16x32_f16 v[10:13], v[18:21], v[2:5], v[10:13]
	ds_read_b128 v[18:21], v40 offset:4480
	ds_read_b128 v[36:39], v40 offset:4544
	s_waitcnt lgkmcnt(1)
	v_mfma_f32_16x16x32_f16 v[44:47], v[18:21], v[2:5], v[22:25]
	ds_read_b128 v[18:21], v40 offset:8832
	ds_read_b128 v[48:51], v40 offset:8896
	s_waitcnt lgkmcnt(1)
	v_mfma_f32_16x16x32_f16 v[28:31], v[18:21], v[2:5], v[28:31]
	ds_read_b128 v[22:25], v40 offset:13184
	ds_read_b128 v[18:21], v40 offset:13248
	s_waitcnt lgkmcnt(1)
	v_mfma_f32_16x16x32_f16 v[22:25], v[22:25], v[2:5], v[6:9]
	v_and_b32_e32 v2, 64, v1
	s_waitcnt vmcnt(0)
	v_mfma_f32_16x16x32_f16 v[10:13], v[32:35], v[14:17], v[10:13]
	v_add_u32_e32 v34, 64, v2
	v_xor_b32_e32 v32, 16, v1
	v_cmp_lt_i32_e32 vcc, v32, v34
	v_mfma_f32_16x16x32_f16 v[6:9], v[36:39], v[14:17], v[44:47]
	v_xor_b32_e32 v33, 32, v1
	v_mfma_f32_16x16x32_f16 v[2:5], v[48:51], v[14:17], v[28:31]
	s_waitcnt lgkmcnt(0)
	v_mfma_f32_16x16x32_f16 v[14:17], v[18:21], v[14:17], v[22:25]
	v_add_f32_e32 v18, 0, v10
	v_mul_f32_e32 v19, v11, v11
	v_add_f32_e32 v18, v18, v11
	v_fmac_f32_e32 v19, v10, v10
	v_add_f32_e32 v18, v18, v12
	v_fmac_f32_e32 v19, v12, v12
	v_add_f32_e32 v18, v18, v13
	v_fmac_f32_e32 v19, v13, v13
	v_add_f32_e32 v18, v18, v6
	v_fmac_f32_e32 v19, v6, v6
	v_add_f32_e32 v18, v18, v7
	v_fmac_f32_e32 v19, v7, v7
	v_add_f32_e32 v18, v18, v8
	v_fmac_f32_e32 v19, v8, v8
	v_add_f32_e32 v18, v18, v9
	v_fmac_f32_e32 v19, v9, v9
	v_add_f32_e32 v18, v18, v2
	v_fmac_f32_e32 v19, v2, v2
	v_add_f32_e32 v18, v18, v3
	v_fmac_f32_e32 v19, v3, v3
	v_add_f32_e32 v18, v18, v4
	v_fmac_f32_e32 v19, v4, v4
	v_add_f32_e32 v18, v18, v5
	v_fmac_f32_e32 v19, v5, v5
	v_add_f32_e32 v18, v18, v14
	v_fmac_f32_e32 v19, v14, v14
	v_add_f32_e32 v18, v18, v15
	v_fmac_f32_e32 v19, v15, v15
	v_cndmask_b32_e32 v28, v1, v32, vcc
	v_add_f32_e32 v18, v18, v16
	v_fmac_f32_e32 v19, v16, v16
	v_lshlrev_b32_e32 v28, 2, v28
	v_add_f32_e32 v18, v18, v17
	v_fmac_f32_e32 v19, v17, v17
	ds_bpermute_b32 v20, v28, v18
	ds_bpermute_b32 v21, v28, v19
	v_cmp_lt_i32_e32 vcc, v33, v34
	s_waitcnt lgkmcnt(1)
	v_add_f32_e32 v18, v18, v20
	v_cndmask_b32_e32 v1, v1, v33, vcc
	v_lshlrev_b32_e32 v1, 2, v1
	s_waitcnt lgkmcnt(0)
	v_add_f32_e32 v19, v19, v21
	ds_bpermute_b32 v20, v1, v18
	ds_bpermute_b32 v21, v1, v19
	v_lshrrev_b32_e32 v1, 6, v0
	v_cmp_eq_u32_e32 vcc, 0, v27
	s_and_saveexec_b64 s[0:1], vcc
	s_cbranch_execz .LBB4_72
	s_lshr_b32 s3, s15, 29
	s_add_i32 s3, s14, s3
	s_and_b32 s3, s3, 0xfffff8
	s_sub_i32 s3, s14, s3
	s_lshl_b32 s4, s3, 8
	s_ashr_i32 s5, s4, 31
	s_lshl_b64 s[4:5], s[4:5], 2
	s_add_u32 s4, s16, s4
	v_lshlrev_b32_e32 v22, 2, v42
	s_addc_u32 s5, s17, s5
	v_lshl_or_b32 v22, v1, 6, v22
	s_waitcnt lgkmcnt(1)
	v_add_f32_e32 v18, v18, v20
	s_waitcnt lgkmcnt(0)
	v_add_f32_e32 v19, v19, v21
	global_atomic_add_f32 v22, v18, s[4:5]
	global_atomic_add_f32 v22, v19, s[4:5] offset:512

_Z12layer_kernelILb0ELi256ELi32EEvPKDv8_DF16_PKfPS0_PiS6_S6_S2_S4_S5_PfPK15HIP_vector_typeIiLj2EEPKi:
	s_setprio 3
	s_load_dword s3, s[0:1], 0x60
	s_load_dwordx2 s[26:27], s[0:1], 0x38
	s_load_dwordx2 s[28:29], s[0:1], 0x0
	s_load_dwordx2 s[14:15], s[0:1], 0x20
	s_load_dwordx2 s[8:9], s[0:1], 0x18
	s_waitcnt lgkmcnt(0)
	s_load_dword s16, s[26:27], 0x0
	s_ashr_i32 s4, s3, 3
	s_and_b32 s5, s3, 7
	s_and_b32 s3, s2, 7
	s_add_i32 s10, s4, 1
	s_cmp_ge_u32 s3, s5
	s_cbranch_scc0 .LBB5_2
	s_mul_i32 s6, s10, s5
	s_sub_i32 s5, s3, s5
	s_mul_i32 s5, s5, s4
	s_add_i32 s11, s6, s5
	s_cbranch_execz .LBB5_3
	s_branch .LBB5_4

.LBB5_24:
	s_setprio 0
	v_or_b32_e32 v46, 1, v35
	v_add_u32_e32 v46, s24, v46
	v_min_i32_e32 v46, 0x1869f, v46
	v_lshl_add_u32 v46, v46, 8, v26
	global_load_dwordx4 v[30:33], v46, s[4:5]
	s_mov_b64 s[22:23], exec
	s_movk_i32 s0, 0x2200
	v_sub_u32_e32 v27, v44, v28
	v_lshl_add_u32 v27, v27, 2, s0
	v_lshl_add_u32 v29, v44, 8, v26
	v_cmp_lt_i32_e64 s[2:3], v44, v45
	v_add_u32_e32 v46, 1, v44
	v_cmp_lt_i32_e64 s[16:17], v46, v45
	v_add_u32_e32 v46, 2, v44
	v_cmp_lt_i32_e64 s[18:19], v46, v45
	v_add_u32_e32 v46, 3, v44
	v_cmp_lt_i32_e64 s[20:21], v46, v45
	s_mov_b64 exec, s[2:3]
	ds_read_b32 v2, v27 offset:0
	global_load_dwordx4 v[4:7], v29, s[12:13] offset:0
	s_waitcnt lgkmcnt(0)
	v_lshl_add_u32 v2, v2, 8, v26
	global_load_dwordx4 v[8:11], v2, s[4:5]
	ds_read_b32 v2, v27 offset:16
	s_mov_b64 exec, s[16:17]
	ds_read_b32 v3, v27 offset:4
	global_load_dwordx4 v[12:15], v29, s[12:13] offset:256
	s_waitcnt lgkmcnt(0)
	v_lshl_add_u32 v3, v3, 8, v26
	global_load_dwordx4 v[16:19], v3, s[4:5]
	ds_read_b32 v3, v27 offset:20
	s_mov_b64 exec, s[18:19]
	ds_read_b32 v24, v27 offset:8
	global_load_dwordx4 v[20:23], v29, s[12:13] offset:512
	s_waitcnt lgkmcnt(0)
	v_lshl_add_u32 v24, v24, 8, v26
	global_load_dwordx4 v[50:53], v24, s[4:5]
	ds_read_b32 v24, v27 offset:24
	s_mov_b64 exec, s[20:21]
	ds_read_b32 v25, v27 offset:12
	global_load_dwordx4 v[54:57], v29, s[12:13] offset:768
	s_waitcnt lgkmcnt(0)
	v_lshl_add_u32 v25, v25, 8, v26
	global_load_dwordx4 v[58:61], v25, s[4:5]
	ds_read_b32 v25, v27 offset:28
	s_mov_b64 exec, s[22:23]
	s_cmp_eq_u64 s[2:3], 0
	s_cbranch_scc1 .Ll1_p1_empty

.LBB5_61:
	s_setprio 3
	v_and_b32_e32 v21, 63, v0
	v_lshrrev_b32_e32 v20, 5, v0
	v_and_b32_e32 v19, 6, v20
	s_waitcnt vmcnt(2)
	v_lshlrev_b32_e32 v2, 4, v21
	v_or_b32_e32 v18, 1, v20
	s_waitcnt vmcnt(1)
	v_lshl_or_b32 v14, v19, 10, v2
	v_lshl_or_b32 v2, v18, 10, v2
	global_load_dwordx4 v[22:25], v14, s[10:11]
	global_load_dwordx4 v[28:31], v2, s[10:11]
	v_or_b32_e32 v2, 0x2000, v14
	global_load_dwordx4 v[36:39], v2, s[10:11]
	v_or_b32_e32 v2, 0x2400, v14
	global_load_dwordx4 v[40:43], v2, s[10:11]
	v_or_b32_e32 v2, 0x4000, v14
	global_load_dwordx4 v[10:13], v2, s[10:11]
	v_or_b32_e32 v2, 0x4400, v14
	global_load_dwordx4 v[6:9], v2, s[10:11]
	v_or_b32_e32 v2, 0x6000, v14
	global_load_dwordx4 v[2:5], v2, s[10:11]
	v_or_b32_e32 v14, 0x6400, v14
	global_load_dwordx4 v[14:17], v14, s[10:11]
	s_movk_i32 s0, 0x110
	v_and_b32_e32 v32, 48, v0
	v_cvt_pk_f16_f32 v51, v50, v51
	v_cvt_pk_f16_f32 v50, v48, v49
	v_cvt_pk_f16_f32 v49, v46, v47
	v_cvt_pk_f16_f32 v48, v34, v35
	v_mad_u32_u24 v27, v27, s0, v26
	v_mad_u32_u24 v60, v1, s0, v32
	ds_write_b128 v27, v[48:51]
	s_waitcnt lgkmcnt(0)
	s_barrier
	ds_read_b128 v[32:35], v60
	ds_read_b128 v[44:47], v60 offset:64
	ds_read_b128 v[52:55], v60 offset:4352
	ds_read_b128 v[56:59], v60 offset:4416
	v_mbcnt_lo_u32_b32 v27, -1, 0
	v_mbcnt_hi_u32_b32 v27, -1, v27
	s_ashr_i32 s0, s25, 31
	s_lshr_b32 s0, s0, 29
	s_add_i32 s0, s25, s0
	s_and_b32 s0, s0, 0xfffff8
	s_sub_i32 s0, s25, s0
	s_lshl_b32 s0, s0, 8
	s_ashr_i32 s1, s0, 31
	s_lshl_b64 s[0:1], s[0:1], 2
	s_add_u32 s0, s8, s0
	s_addc_u32 s1, s9, s1
	s_waitcnt vmcnt(7) lgkmcnt(3)
	v_mfma_f32_16x16x32_f16 v[48:51], v[32:35], v[22:25], 0
	s_waitcnt vmcnt(6)
	v_mfma_f32_16x16x32_f16 v[32:35], v[32:35], v[28:31], 0
	s_waitcnt lgkmcnt(1)
	v_mfma_f32_16x16x32_f16 v[22:25], v[52:55], v[22:25], 0
	v_mfma_f32_16x16x32_f16 v[28:31], v[52:55], v[28:31], 0
	s_waitcnt vmcnt(5)
	v_mfma_f32_16x16x32_f16 v[48:51], v[44:47], v[36:39], v[48:51]
	s_waitcnt vmcnt(4)
	v_mfma_f32_16x16x32_f16 v[32:35], v[44:47], v[40:43], v[32:35]
	s_waitcnt lgkmcnt(0)
	v_mfma_f32_16x16x32_f16 v[22:25], v[56:59], v[36:39], v[22:25]
	v_mfma_f32_16x16x32_f16 v[28:31], v[56:59], v[40:43], v[28:31]
	ds_read_b128 v[36:39], v60 offset:128
	ds_read_b128 v[40:43], v60 offset:4480
	ds_read_b128 v[44:47], v60 offset:192
	s_waitcnt vmcnt(3) lgkmcnt(2)
	v_mfma_f32_16x16x32_f16 v[48:51], v[36:39], v[10:13], v[48:51]
	s_waitcnt vmcnt(2)
	v_mfma_f32_16x16x32_f16 v[32:35], v[36:39], v[6:9], v[32:35]
	ds_read_b128 v[36:39], v60 offset:4544
	s_waitcnt lgkmcnt(2)
	v_mfma_f32_16x16x32_f16 v[52:55], v[40:43], v[10:13], v[22:25]
	v_and_b32_e32 v10, 64, v27
	s_nop 1
	v_xor_b32_e32 v22, 16, v27
	v_mfma_f32_16x16x32_f16 v[28:31], v[40:43], v[6:9], v[28:31]
	v_add_u32_e32 v6, 64, v10
	v_xor_b32_e32 v23, 32, v27
	v_cmp_lt_i32_e32 vcc, v22, v6
	s_waitcnt vmcnt(1) lgkmcnt(1)
	v_mfma_f32_16x16x32_f16 v[10:13], v[44:47], v[2:5], v[48:51]
	v_cndmask_b32_e32 v22, v27, v22, vcc
	v_cmp_lt_i32_e32 vcc, v23, v6
	s_waitcnt lgkmcnt(0)
	v_mfma_f32_16x16x32_f16 v[2:5], v[36:39], v[2:5], v[52:55]
	v_cndmask_b32_e32 v24, v27, v23, vcc
	v_lshlrev_b32_e32 v23, 2, v22
	v_lshlrev_b32_e32 v22, 2, v24
	s_nop 0
	v_add_f32_e32 v24, 0, v10
	v_mul_f32_e32 v25, v11, v11
	v_add_f32_e32 v24, v24, v11
	v_fmac_f32_e32 v25, v10, v10
	v_add_f32_e32 v24, v24, v12
	v_fmac_f32_e32 v25, v12, v12
	v_add_f32_e32 v24, v24, v13
	v_fmac_f32_e32 v25, v13, v13
	v_add_f32_e32 v24, v24, v2
	v_fmac_f32_e32 v25, v2, v2
	v_add_f32_e32 v24, v24, v3
	v_fmac_f32_e32 v25, v3, v3
	v_add_f32_e32 v24, v24, v4
	v_fmac_f32_e32 v25, v4, v4
	v_add_f32_e32 v24, v24, v5
	v_fmac_f32_e32 v25, v5, v5
	s_waitcnt vmcnt(0)
	v_mfma_f32_16x16x32_f16 v[6:9], v[44:47], v[14:17], v[32:35]
	ds_bpermute_b32 v27, v23, v24
	v_cmp_gt_u32_e32 vcc, 16, v21
	v_lshlrev_b32_e32 v21, 2, v1
	ds_bpermute_b32 v32, v23, v25
	v_mfma_f32_16x16x32_f16 v[14:17], v[36:39], v[14:17], v[28:31]
	s_waitcnt lgkmcnt(1)
	v_add_f32_e32 v24, v24, v27
	ds_bpermute_b32 v27, v22, v24
	s_waitcnt lgkmcnt(1)
	v_add_f32_e32 v25, v25, v32
	ds_bpermute_b32 v28, v22, v25
	s_and_saveexec_b64 s[2:3], vcc
	s_cbranch_execz .LBB5_63
	s_waitcnt lgkmcnt(1)
	v_add_f32_e32 v24, v24, v27
	v_lshl_or_b32 v27, v19, 6, v21
	s_waitcnt lgkmcnt(0)
	v_add_f32_e32 v25, v25, v28
	global_atomic_add_f32 v27, v24, s[0:1]
	global_atomic_add_f32 v27, v25, s[0:1] offset:512
